# v21 plus half-0 softmax woven into half-1 QK MFMA stream
# speedup vs baseline: 1.0280x; 1.0019x over previous
.LBB0_556:
	s_cmp_le_i32 s63, s28
	s_cbranch_scc0 .Lorig_a0b0
	s_cmp_eq_u32 s17, 0
	s_cbranch_scc1 .Lorig_a0b0
	s_setprio 3
	ds_read_b128 v[116:119], v189 offset:0
	ds_read_b128 v[120:123], v226 offset:0
	ds_read_b128 v[124:127], v227 offset:0
	ds_read_b128 v[128:131], v228 offset:0
	s_waitcnt lgkmcnt(3)
	v_mfma_f32_32x32x16_bf16 v[84:99], v[116:119], v[132:135], 0
	ds_read_b128 v[116:119], v232 offset:0
	s_waitcnt lgkmcnt(3)
	v_mfma_f32_32x32x16_bf16 v[84:99], v[120:123], v[136:139], v[84:99]
	ds_read_b128 v[120:123], v233 offset:0
	s_waitcnt lgkmcnt(3)
	v_mfma_f32_32x32x16_bf16 v[84:99], v[124:127], v[140:143], v[84:99]
	ds_read_b128 v[124:127], v234 offset:0
	s_waitcnt lgkmcnt(3)
	v_mfma_f32_32x32x16_bf16 v[84:99], v[128:131], v[144:147], v[84:99]
	ds_read_b128 v[128:131], v235 offset:0
	s_waitcnt lgkmcnt(3)
	v_mfma_f32_32x32x16_bf16 v[84:99], v[116:119], v[148:151], v[84:99]
	ds_read_b128 v[116:119], v190 offset:0
	s_waitcnt lgkmcnt(3)
	v_mfma_f32_32x32x16_bf16 v[84:99], v[120:123], v[152:155], v[84:99]
	ds_read_b128 v[120:123], v229 offset:0
	s_waitcnt lgkmcnt(3)
	v_mfma_f32_32x32x16_bf16 v[84:99], v[124:127], v[156:159], v[84:99]
	ds_read_b128 v[124:127], v230 offset:0
	s_waitcnt lgkmcnt(3)
	v_mfma_f32_32x32x16_bf16 v[84:99], v[128:131], v[160:163], v[84:99]
	ds_read_b128 v[128:131], v231 offset:0
	s_waitcnt lgkmcnt(3)
	v_mfma_f32_32x32x16_bf16 v[84:99], v[116:119], v[164:167], v[84:99]
	ds_read_b128 v[116:119], v189 offset:8192
	s_waitcnt lgkmcnt(3)
	v_mfma_f32_32x32x16_bf16 v[84:99], v[120:123], v[172:175], v[84:99]
	ds_read_b128 v[120:123], v226 offset:8192
	s_waitcnt lgkmcnt(3)
	v_mfma_f32_32x32x16_bf16 v[84:99], v[124:127], v[168:171], v[84:99]
	ds_read_b128 v[124:127], v227 offset:8192
	s_waitcnt lgkmcnt(3)
	v_mfma_f32_32x32x16_bf16 v[84:99], v[128:131], v[176:179], v[84:99]
	ds_read_b128 v[128:131], v228 offset:8192
	v_cmp_eq_f32_e32 vcc, 0, v223
	s_cmp_eq_u64 vcc, exec
	s_cbranch_scc0 .Lsub_a0b0
	s_waitcnt lgkmcnt(3)
	v_mfma_f32_32x32x16_bf16 v[68:83], v[116:119], v[132:135], 0
	ds_read_b128 v[116:119], v232 offset:8192
	s_waitcnt lgkmcnt(3)
	v_mfma_f32_32x32x16_bf16 v[68:83], v[120:123], v[136:139], v[68:83]
	ds_read_b128 v[120:123], v233 offset:8192
	s_waitcnt lgkmcnt(3)
	v_mfma_f32_32x32x16_bf16 v[68:83], v[124:127], v[140:143], v[68:83]
	ds_read_b128 v[124:127], v234 offset:8192
	s_waitcnt lgkmcnt(3)
	v_mfma_f32_32x32x16_bf16 v[68:83], v[128:131], v[144:147], v[68:83]
	ds_read_b128 v[128:131], v235 offset:8192
	s_waitcnt lgkmcnt(3)
	v_mfma_f32_32x32x16_bf16 v[68:83], v[116:119], v[148:151], v[68:83]
	ds_read_b128 v[116:119], v190 offset:4096
	v_exp_f32_e32 v100, v84
	v_exp_f32_e32 v101, v85
	v_exp_f32_e32 v102, v86
	v_exp_f32_e32 v103, v87
	v_exp_f32_e32 v104, v88
	v_exp_f32_e32 v105, v89
	s_waitcnt lgkmcnt(3)
	v_mfma_f32_32x32x16_bf16 v[68:83], v[120:123], v[152:155], v[68:83]
	ds_read_b128 v[120:123], v229 offset:4096
	v_exp_f32_e32 v106, v90
	v_exp_f32_e32 v107, v91
	v_exp_f32_e32 v108, v92
	v_exp_f32_e32 v109, v93
	v_exp_f32_e32 v110, v94
	v_exp_f32_e32 v111, v95
	s_waitcnt lgkmcnt(3)
	v_mfma_f32_32x32x16_bf16 v[68:83], v[124:127], v[156:159], v[68:83]
	ds_read_b128 v[124:127], v230 offset:4096
	v_exp_f32_e32 v112, v96
	v_exp_f32_e32 v113, v97
	v_exp_f32_e32 v114, v98
	v_exp_f32_e32 v115, v99
	v_add_f32_e32 v237, v100, v101
	v_add_f32_e32 v251, v102, v103
	s_waitcnt lgkmcnt(3)
	v_mfma_f32_32x32x16_bf16 v[68:83], v[128:131], v[160:163], v[68:83]
	ds_read_b128 v[128:131], v231 offset:4096
	v_add_f32_e32 v237, v237, v104
	v_add_f32_e32 v251, v251, v105
	v_add_f32_e32 v237, v237, v106
	v_add_f32_e32 v251, v251, v107
	v_add_f32_e32 v237, v237, v108
	v_add_f32_e32 v251, v251, v109
	s_waitcnt lgkmcnt(3)
	v_mfma_f32_32x32x16_bf16 v[68:83], v[116:119], v[164:167], v[68:83]
	v_add_f32_e32 v237, v237, v110
	v_add_f32_e32 v251, v251, v111
	v_add_f32_e32 v237, v237, v112
	v_add_f32_e32 v251, v251, v113
	v_add_f32_e32 v237, v237, v114
	v_add_f32_e32 v251, v251, v115
	s_waitcnt lgkmcnt(2)
	v_mfma_f32_32x32x16_bf16 v[68:83], v[120:123], v[172:175], v[68:83]
	v_add_f32_e32 v237, v237, v251
	v_cvt_pk_bf16_f32 v238, v100, v101
	v_cvt_pk_bf16_f32 v239, v102, v103
	v_cvt_pk_bf16_f32 v240, v104, v105
	v_cvt_pk_bf16_f32 v241, v106, v107
	v_cvt_pk_bf16_f32 v242, v108, v109
	s_waitcnt lgkmcnt(1)
	v_mfma_f32_32x32x16_bf16 v[68:83], v[124:127], v[168:171], v[68:83]
	v_cvt_pk_bf16_f32 v243, v110, v111
	v_cvt_pk_bf16_f32 v244, v112, v113
	v_cvt_pk_bf16_f32 v245, v114, v115
	s_nop 1
	v_permlane32_swap_b32_e32 v238, v240
	v_permlane32_swap_b32_e32 v239, v241
	s_waitcnt lgkmcnt(0)
	v_mfma_f32_32x32x16_bf16 v[68:83], v[128:131], v[176:179], v[68:83]
	v_permlane32_swap_b32_e32 v242, v244
	v_permlane32_swap_b32_e32 v243, v245
	ds_read_b64_tr_b16 v[116:117], v191 offset:0
	ds_read_b64_tr_b16 v[118:119], v191 offset:2048
	ds_read_b64_tr_b16 v[120:121], v191 offset:4096
	ds_read_b64_tr_b16 v[122:123], v191 offset:6144
	ds_read_b64_tr_b16 v[124:125], v191 offset:8192
	ds_read_b64_tr_b16 v[126:127], v191 offset:10240
	ds_read_b64_tr_b16 v[128:129], v191 offset:12288
	ds_read_b64_tr_b16 v[130:131], v191 offset:14336
	s_setprio 0
	s_nop 3
	v_exp_f32_e32 v100, v68
	v_exp_f32_e32 v101, v69
	v_exp_f32_e32 v102, v70
	v_exp_f32_e32 v103, v71
	v_exp_f32_e32 v104, v72
	v_exp_f32_e32 v105, v73
	v_exp_f32_e32 v106, v74
	v_exp_f32_e32 v107, v75
	v_exp_f32_e32 v108, v76
	v_exp_f32_e32 v109, v77
	v_exp_f32_e32 v110, v78
	v_exp_f32_e32 v111, v79
	v_exp_f32_e32 v112, v80
	v_exp_f32_e32 v113, v81
	v_exp_f32_e32 v114, v82
	v_exp_f32_e32 v115, v83
	v_add_f32_e32 v250, v100, v101
	v_add_f32_e32 v251, v102, v103
	v_add_f32_e32 v250, v250, v104
	v_add_f32_e32 v251, v251, v105
	v_add_f32_e32 v250, v250, v106
	v_add_f32_e32 v251, v251, v107
	v_add_f32_e32 v250, v250, v108
	v_add_f32_e32 v251, v251, v109
	v_add_f32_e32 v250, v250, v110
	v_add_f32_e32 v251, v251, v111
	v_add_f32_e32 v250, v250, v112
	v_add_f32_e32 v251, v251, v113
	v_add_f32_e32 v250, v250, v114
	v_add_f32_e32 v251, v251, v115
	v_add_f32_e32 v250, v250, v251
	v_cvt_pk_bf16_f32 v100, v100, v101
	v_cvt_pk_bf16_f32 v101, v102, v103
	v_cvt_pk_bf16_f32 v102, v104, v105
	v_cvt_pk_bf16_f32 v103, v106, v107
	v_cvt_pk_bf16_f32 v104, v108, v109
	v_cvt_pk_bf16_f32 v105, v110, v111
	v_cvt_pk_bf16_f32 v106, v112, v113
	v_cvt_pk_bf16_f32 v107, v114, v115
	s_nop 1
	v_permlane32_swap_b32_e32 v100, v102
	v_permlane32_swap_b32_e32 v101, v103
	v_permlane32_swap_b32_e32 v104, v106
	v_permlane32_swap_b32_e32 v105, v107
	s_branch .Lsum_a0b0
.Lsub_a0b0:
	s_waitcnt lgkmcnt(3)
	v_mfma_f32_32x32x16_bf16 v[68:83], v[116:119], v[132:135], 0
	ds_read_b128 v[116:119], v232 offset:8192
	s_waitcnt lgkmcnt(3)
	v_mfma_f32_32x32x16_bf16 v[68:83], v[120:123], v[136:139], v[68:83]
	ds_read_b128 v[120:123], v233 offset:8192
	s_waitcnt lgkmcnt(3)
	v_mfma_f32_32x32x16_bf16 v[68:83], v[124:127], v[140:143], v[68:83]
	ds_read_b128 v[124:127], v234 offset:8192
	s_waitcnt lgkmcnt(3)
	v_mfma_f32_32x32x16_bf16 v[68:83], v[128:131], v[144:147], v[68:83]
	ds_read_b128 v[128:131], v235 offset:8192
	s_waitcnt lgkmcnt(3)
	v_mfma_f32_32x32x16_bf16 v[68:83], v[116:119], v[148:151], v[68:83]
	ds_read_b128 v[116:119], v190 offset:4096
	v_sub_f32_e32 v100, v84, v223
	v_sub_f32_e32 v101, v85, v223
	v_sub_f32_e32 v102, v86, v223
	v_sub_f32_e32 v103, v87, v223
	v_sub_f32_e32 v104, v88, v223
	v_sub_f32_e32 v105, v89, v223
	v_sub_f32_e32 v106, v90, v223
	v_sub_f32_e32 v107, v91, v223
	s_waitcnt lgkmcnt(3)
	v_mfma_f32_32x32x16_bf16 v[68:83], v[120:123], v[152:155], v[68:83]
	ds_read_b128 v[120:123], v229 offset:4096
	v_sub_f32_e32 v108, v92, v223
	v_sub_f32_e32 v109, v93, v223
	v_sub_f32_e32 v110, v94, v223
	v_sub_f32_e32 v111, v95, v223
	v_sub_f32_e32 v112, v96, v223
	v_sub_f32_e32 v113, v97, v223
	v_sub_f32_e32 v114, v98, v223
	v_sub_f32_e32 v115, v99, v223
	s_waitcnt lgkmcnt(3)
	v_mfma_f32_32x32x16_bf16 v[68:83], v[124:127], v[156:159], v[68:83]
	ds_read_b128 v[124:127], v230 offset:4096
	v_exp_f32_e32 v100, v100
	v_exp_f32_e32 v101, v101
	v_exp_f32_e32 v102, v102
	v_exp_f32_e32 v103, v103
	v_exp_f32_e32 v104, v104
	v_exp_f32_e32 v105, v105
	v_exp_f32_e32 v106, v106
	v_exp_f32_e32 v107, v107
	s_waitcnt lgkmcnt(3)
	v_mfma_f32_32x32x16_bf16 v[68:83], v[128:131], v[160:163], v[68:83]
	ds_read_b128 v[128:131], v231 offset:4096
	v_exp_f32_e32 v108, v108
	v_exp_f32_e32 v109, v109
	v_exp_f32_e32 v110, v110
	v_exp_f32_e32 v111, v111
	v_exp_f32_e32 v112, v112
	v_exp_f32_e32 v113, v113
	v_exp_f32_e32 v114, v114
	v_exp_f32_e32 v115, v115
	s_waitcnt lgkmcnt(3)
	v_mfma_f32_32x32x16_bf16 v[68:83], v[116:119], v[164:167], v[68:83]
	v_add_f32_e32 v237, v100, v101
	v_add_f32_e32 v251, v102, v103
	v_add_f32_e32 v237, v237, v104
	v_add_f32_e32 v251, v251, v105
	v_add_f32_e32 v237, v237, v106
	v_add_f32_e32 v251, v251, v107
	v_add_f32_e32 v237, v237, v108
	v_add_f32_e32 v251, v251, v109
	s_waitcnt lgkmcnt(2)
	v_mfma_f32_32x32x16_bf16 v[68:83], v[120:123], v[172:175], v[68:83]
	v_add_f32_e32 v237, v237, v110
	v_add_f32_e32 v251, v251, v111
	v_add_f32_e32 v237, v237, v112
	v_add_f32_e32 v251, v251, v113
	v_add_f32_e32 v237, v237, v114
	v_add_f32_e32 v251, v251, v115
	v_add_f32_e32 v237, v237, v251
	v_cvt_pk_bf16_f32 v238, v100, v101
	s_waitcnt lgkmcnt(1)
	v_mfma_f32_32x32x16_bf16 v[68:83], v[124:127], v[168:171], v[68:83]
	v_cvt_pk_bf16_f32 v239, v102, v103
	v_cvt_pk_bf16_f32 v240, v104, v105
	v_cvt_pk_bf16_f32 v241, v106, v107
	v_cvt_pk_bf16_f32 v242, v108, v109
	v_cvt_pk_bf16_f32 v243, v110, v111
	v_cvt_pk_bf16_f32 v244, v112, v113
	v_cvt_pk_bf16_f32 v245, v114, v115
	s_nop 1
	s_waitcnt lgkmcnt(0)
	v_mfma_f32_32x32x16_bf16 v[68:83], v[128:131], v[176:179], v[68:83]
	v_permlane32_swap_b32_e32 v238, v240
	v_permlane32_swap_b32_e32 v239, v241
	v_permlane32_swap_b32_e32 v242, v244
	v_permlane32_swap_b32_e32 v243, v245
	ds_read_b64_tr_b16 v[116:117], v191 offset:0
	ds_read_b64_tr_b16 v[118:119], v191 offset:2048
	ds_read_b64_tr_b16 v[120:121], v191 offset:4096
	ds_read_b64_tr_b16 v[122:123], v191 offset:6144
	ds_read_b64_tr_b16 v[124:125], v191 offset:8192
	ds_read_b64_tr_b16 v[126:127], v191 offset:10240
	ds_read_b64_tr_b16 v[128:129], v191 offset:12288
	ds_read_b64_tr_b16 v[130:131], v191 offset:14336
	s_setprio 0
	s_nop 3
	v_sub_f32_e32 v100, v68, v223
	v_sub_f32_e32 v101, v69, v223
	v_sub_f32_e32 v102, v70, v223
	v_sub_f32_e32 v103, v71, v223
	v_sub_f32_e32 v104, v72, v223
	v_sub_f32_e32 v105, v73, v223
	v_sub_f32_e32 v106, v74, v223
	v_sub_f32_e32 v107, v75, v223
	v_sub_f32_e32 v108, v76, v223
	v_sub_f32_e32 v109, v77, v223
	v_sub_f32_e32 v110, v78, v223
	v_sub_f32_e32 v111, v79, v223
	v_sub_f32_e32 v112, v80, v223
	v_sub_f32_e32 v113, v81, v223
	v_sub_f32_e32 v114, v82, v223
	v_sub_f32_e32 v115, v83, v223
	v_exp_f32_e32 v100, v100
	v_exp_f32_e32 v101, v101
	v_exp_f32_e32 v102, v102
	v_exp_f32_e32 v103, v103
	v_exp_f32_e32 v104, v104
	v_exp_f32_e32 v105, v105
	v_exp_f32_e32 v106, v106
	v_exp_f32_e32 v107, v107
	v_exp_f32_e32 v108, v108
	v_exp_f32_e32 v109, v109
	v_exp_f32_e32 v110, v110
	v_exp_f32_e32 v111, v111
	v_exp_f32_e32 v112, v112
	v_exp_f32_e32 v113, v113
	v_exp_f32_e32 v114, v114
	v_exp_f32_e32 v115, v115
	v_add_f32_e32 v250, v100, v101
	v_add_f32_e32 v251, v102, v103
	v_add_f32_e32 v250, v250, v104
	v_add_f32_e32 v251, v251, v105
	v_add_f32_e32 v250, v250, v106
	v_add_f32_e32 v251, v251, v107
	v_add_f32_e32 v250, v250, v108
	v_add_f32_e32 v251, v251, v109
	v_add_f32_e32 v250, v250, v110
	v_add_f32_e32 v251, v251, v111
	v_add_f32_e32 v250, v250, v112
	v_add_f32_e32 v251, v251, v113
	v_add_f32_e32 v250, v250, v114
	v_add_f32_e32 v251, v251, v115
	v_add_f32_e32 v250, v250, v251
	v_cvt_pk_bf16_f32 v100, v100, v101
	v_cvt_pk_bf16_f32 v101, v102, v103
	v_cvt_pk_bf16_f32 v102, v104, v105
	v_cvt_pk_bf16_f32 v103, v106, v107
	v_cvt_pk_bf16_f32 v104, v108, v109
	v_cvt_pk_bf16_f32 v105, v110, v111
	v_cvt_pk_bf16_f32 v106, v112, v113
	v_cvt_pk_bf16_f32 v107, v114, v115
	s_nop 1
	v_permlane32_swap_b32_e32 v100, v102
	v_permlane32_swap_b32_e32 v101, v103
	v_permlane32_swap_b32_e32 v104, v106
	v_permlane32_swap_b32_e32 v105, v107

.LBB0_571:
	s_add_i32 s98, s63, 64
	s_cmp_le_i32 s98, s28
	s_cbranch_scc0 .Lorig_a0b1
	s_setprio 3
	ds_read_b128 v[116:119], v189 offset:24576
	ds_read_b128 v[120:123], v226 offset:24576
	ds_read_b128 v[124:127], v227 offset:24576
	ds_read_b128 v[128:131], v228 offset:24576
	s_waitcnt lgkmcnt(3)
	v_mfma_f32_32x32x16_bf16 v[84:99], v[116:119], v[132:135], 0
	ds_read_b128 v[116:119], v232 offset:24576
	s_waitcnt lgkmcnt(3)
	v_mfma_f32_32x32x16_bf16 v[84:99], v[120:123], v[136:139], v[84:99]
	ds_read_b128 v[120:123], v233 offset:24576
	s_waitcnt lgkmcnt(3)
	v_mfma_f32_32x32x16_bf16 v[84:99], v[124:127], v[140:143], v[84:99]
	ds_read_b128 v[124:127], v234 offset:24576
	s_waitcnt lgkmcnt(3)
	v_mfma_f32_32x32x16_bf16 v[84:99], v[128:131], v[144:147], v[84:99]
	ds_read_b128 v[128:131], v235 offset:24576
	s_waitcnt lgkmcnt(3)
	v_mfma_f32_32x32x16_bf16 v[84:99], v[116:119], v[148:151], v[84:99]
	ds_read_b128 v[116:119], v190 offset:24576
	s_waitcnt lgkmcnt(3)
	v_mfma_f32_32x32x16_bf16 v[84:99], v[120:123], v[152:155], v[84:99]
	ds_read_b128 v[120:123], v229 offset:24576
	s_waitcnt lgkmcnt(3)
	v_mfma_f32_32x32x16_bf16 v[84:99], v[124:127], v[156:159], v[84:99]
	ds_read_b128 v[124:127], v230 offset:24576
	s_waitcnt lgkmcnt(3)
	v_mfma_f32_32x32x16_bf16 v[84:99], v[128:131], v[160:163], v[84:99]
	ds_read_b128 v[128:131], v231 offset:24576
	s_waitcnt lgkmcnt(3)
	v_mfma_f32_32x32x16_bf16 v[84:99], v[116:119], v[164:167], v[84:99]
	ds_read_b128 v[116:119], v189 offset:32768
	s_waitcnt lgkmcnt(3)
	v_mfma_f32_32x32x16_bf16 v[84:99], v[120:123], v[172:175], v[84:99]
	ds_read_b128 v[120:123], v226 offset:32768
	s_waitcnt lgkmcnt(3)
	v_mfma_f32_32x32x16_bf16 v[84:99], v[124:127], v[168:171], v[84:99]
	ds_read_b128 v[124:127], v227 offset:32768
	s_waitcnt lgkmcnt(3)
	v_mfma_f32_32x32x16_bf16 v[84:99], v[128:131], v[176:179], v[84:99]
	ds_read_b128 v[128:131], v228 offset:32768
	v_cmp_eq_f32_e32 vcc, 0, v222
	s_cmp_eq_u64 vcc, exec
	s_cbranch_scc0 .Lsub_a0b1
	s_waitcnt lgkmcnt(3)
	v_mfma_f32_32x32x16_bf16 v[68:83], v[116:119], v[132:135], 0
	ds_read_b128 v[116:119], v232 offset:32768
	s_waitcnt lgkmcnt(3)
	v_mfma_f32_32x32x16_bf16 v[68:83], v[120:123], v[136:139], v[68:83]
	ds_read_b128 v[120:123], v233 offset:32768
	s_waitcnt lgkmcnt(3)
	v_mfma_f32_32x32x16_bf16 v[68:83], v[124:127], v[140:143], v[68:83]
	ds_read_b128 v[124:127], v234 offset:32768
	s_waitcnt lgkmcnt(3)
	v_mfma_f32_32x32x16_bf16 v[68:83], v[128:131], v[144:147], v[68:83]
	ds_read_b128 v[128:131], v235 offset:32768
	s_waitcnt lgkmcnt(3)
	v_mfma_f32_32x32x16_bf16 v[68:83], v[116:119], v[148:151], v[68:83]
	ds_read_b128 v[116:119], v190 offset:28672
	v_exp_f32_e32 v100, v84
	v_exp_f32_e32 v101, v85
	v_exp_f32_e32 v102, v86
	v_exp_f32_e32 v103, v87
	v_exp_f32_e32 v104, v88
	v_exp_f32_e32 v105, v89
	s_waitcnt lgkmcnt(3)
	v_mfma_f32_32x32x16_bf16 v[68:83], v[120:123], v[152:155], v[68:83]
	ds_read_b128 v[120:123], v229 offset:28672
	v_exp_f32_e32 v106, v90
	v_exp_f32_e32 v107, v91
	v_exp_f32_e32 v108, v92
	v_exp_f32_e32 v109, v93
	v_exp_f32_e32 v110, v94
	v_exp_f32_e32 v111, v95
	s_waitcnt lgkmcnt(3)
	v_mfma_f32_32x32x16_bf16 v[68:83], v[124:127], v[156:159], v[68:83]
	ds_read_b128 v[124:127], v230 offset:28672
	v_exp_f32_e32 v112, v96
	v_exp_f32_e32 v113, v97
	v_exp_f32_e32 v114, v98
	v_exp_f32_e32 v115, v99
	v_add_f32_e32 v237, v100, v101
	v_add_f32_e32 v251, v102, v103
	s_waitcnt lgkmcnt(3)
	v_mfma_f32_32x32x16_bf16 v[68:83], v[128:131], v[160:163], v[68:83]
	ds_read_b128 v[128:131], v231 offset:28672
	v_add_f32_e32 v237, v237, v104
	v_add_f32_e32 v251, v251, v105
	v_add_f32_e32 v237, v237, v106
	v_add_f32_e32 v251, v251, v107
	v_add_f32_e32 v237, v237, v108
	v_add_f32_e32 v251, v251, v109
	s_waitcnt lgkmcnt(3)
	v_mfma_f32_32x32x16_bf16 v[68:83], v[116:119], v[164:167], v[68:83]
	v_add_f32_e32 v237, v237, v110
	v_add_f32_e32 v251, v251, v111
	v_add_f32_e32 v237, v237, v112
	v_add_f32_e32 v251, v251, v113
	v_add_f32_e32 v237, v237, v114
	v_add_f32_e32 v251, v251, v115
	s_waitcnt lgkmcnt(2)
	v_mfma_f32_32x32x16_bf16 v[68:83], v[120:123], v[172:175], v[68:83]
	v_add_f32_e32 v237, v237, v251
	v_cvt_pk_bf16_f32 v238, v100, v101
	v_cvt_pk_bf16_f32 v239, v102, v103
	v_cvt_pk_bf16_f32 v240, v104, v105
	v_cvt_pk_bf16_f32 v241, v106, v107
	v_cvt_pk_bf16_f32 v242, v108, v109
	s_waitcnt lgkmcnt(1)
	v_mfma_f32_32x32x16_bf16 v[68:83], v[124:127], v[168:171], v[68:83]
	v_cvt_pk_bf16_f32 v243, v110, v111
	v_cvt_pk_bf16_f32 v244, v112, v113
	v_cvt_pk_bf16_f32 v245, v114, v115
	s_nop 1
	v_permlane32_swap_b32_e32 v238, v240
	v_permlane32_swap_b32_e32 v239, v241
	s_waitcnt lgkmcnt(0)
	v_mfma_f32_32x32x16_bf16 v[68:83], v[128:131], v[176:179], v[68:83]
	v_permlane32_swap_b32_e32 v242, v244
	v_permlane32_swap_b32_e32 v243, v245
	ds_read_b64_tr_b16 v[116:117], v191 offset:16384
	ds_read_b64_tr_b16 v[118:119], v191 offset:18432
	ds_read_b64_tr_b16 v[120:121], v191 offset:20480
	ds_read_b64_tr_b16 v[122:123], v191 offset:22528
	ds_read_b64_tr_b16 v[124:125], v191 offset:24576
	ds_read_b64_tr_b16 v[126:127], v191 offset:26624
	ds_read_b64_tr_b16 v[128:129], v191 offset:28672
	ds_read_b64_tr_b16 v[130:131], v191 offset:30720
	s_setprio 0
	s_nop 3
	v_exp_f32_e32 v100, v68
	v_exp_f32_e32 v101, v69
	v_exp_f32_e32 v102, v70
	v_exp_f32_e32 v103, v71
	v_exp_f32_e32 v104, v72
	v_exp_f32_e32 v105, v73
	v_exp_f32_e32 v106, v74
	v_exp_f32_e32 v107, v75
	v_exp_f32_e32 v108, v76
	v_exp_f32_e32 v109, v77
	v_exp_f32_e32 v110, v78
	v_exp_f32_e32 v111, v79
	v_exp_f32_e32 v112, v80
	v_exp_f32_e32 v113, v81
	v_exp_f32_e32 v114, v82
	v_exp_f32_e32 v115, v83
	v_add_f32_e32 v250, v100, v101
	v_add_f32_e32 v251, v102, v103
	v_add_f32_e32 v250, v250, v104
	v_add_f32_e32 v251, v251, v105
	v_add_f32_e32 v250, v250, v106
	v_add_f32_e32 v251, v251, v107
	v_add_f32_e32 v250, v250, v108
	v_add_f32_e32 v251, v251, v109
	v_add_f32_e32 v250, v250, v110
	v_add_f32_e32 v251, v251, v111
	v_add_f32_e32 v250, v250, v112
	v_add_f32_e32 v251, v251, v113
	v_add_f32_e32 v250, v250, v114
	v_add_f32_e32 v251, v251, v115
	v_add_f32_e32 v250, v250, v251
	v_cvt_pk_bf16_f32 v100, v100, v101
	v_cvt_pk_bf16_f32 v101, v102, v103
	v_cvt_pk_bf16_f32 v102, v104, v105
	v_cvt_pk_bf16_f32 v103, v106, v107
	v_cvt_pk_bf16_f32 v104, v108, v109
	v_cvt_pk_bf16_f32 v105, v110, v111
	v_cvt_pk_bf16_f32 v106, v112, v113
	v_cvt_pk_bf16_f32 v107, v114, v115
	s_nop 1
	v_permlane32_swap_b32_e32 v100, v102
	v_permlane32_swap_b32_e32 v101, v103
	v_permlane32_swap_b32_e32 v104, v106
	v_permlane32_swap_b32_e32 v105, v107
	s_branch .Lsum_a0b1
.Lsub_a0b1:
	s_waitcnt lgkmcnt(3)
	v_mfma_f32_32x32x16_bf16 v[68:83], v[116:119], v[132:135], 0
	ds_read_b128 v[116:119], v232 offset:32768
	s_waitcnt lgkmcnt(3)
	v_mfma_f32_32x32x16_bf16 v[68:83], v[120:123], v[136:139], v[68:83]
	ds_read_b128 v[120:123], v233 offset:32768
	s_waitcnt lgkmcnt(3)
	v_mfma_f32_32x32x16_bf16 v[68:83], v[124:127], v[140:143], v[68:83]
	ds_read_b128 v[124:127], v234 offset:32768
	s_waitcnt lgkmcnt(3)
	v_mfma_f32_32x32x16_bf16 v[68:83], v[128:131], v[144:147], v[68:83]
	ds_read_b128 v[128:131], v235 offset:32768
	s_waitcnt lgkmcnt(3)
	v_mfma_f32_32x32x16_bf16 v[68:83], v[116:119], v[148:151], v[68:83]
	ds_read_b128 v[116:119], v190 offset:28672
	v_sub_f32_e32 v100, v84, v222
	v_sub_f32_e32 v101, v85, v222
	v_sub_f32_e32 v102, v86, v222
	v_sub_f32_e32 v103, v87, v222
	v_sub_f32_e32 v104, v88, v222
	v_sub_f32_e32 v105, v89, v222
	v_sub_f32_e32 v106, v90, v222
	v_sub_f32_e32 v107, v91, v222
	s_waitcnt lgkmcnt(3)
	v_mfma_f32_32x32x16_bf16 v[68:83], v[120:123], v[152:155], v[68:83]
	ds_read_b128 v[120:123], v229 offset:28672
	v_sub_f32_e32 v108, v92, v222
	v_sub_f32_e32 v109, v93, v222
	v_sub_f32_e32 v110, v94, v222
	v_sub_f32_e32 v111, v95, v222
	v_sub_f32_e32 v112, v96, v222
	v_sub_f32_e32 v113, v97, v222
	v_sub_f32_e32 v114, v98, v222
	v_sub_f32_e32 v115, v99, v222
	s_waitcnt lgkmcnt(3)
	v_mfma_f32_32x32x16_bf16 v[68:83], v[124:127], v[156:159], v[68:83]
	ds_read_b128 v[124:127], v230 offset:28672
	v_exp_f32_e32 v100, v100
	v_exp_f32_e32 v101, v101
	v_exp_f32_e32 v102, v102
	v_exp_f32_e32 v103, v103
	v_exp_f32_e32 v104, v104
	v_exp_f32_e32 v105, v105
	v_exp_f32_e32 v106, v106
	v_exp_f32_e32 v107, v107
	s_waitcnt lgkmcnt(3)
	v_mfma_f32_32x32x16_bf16 v[68:83], v[128:131], v[160:163], v[68:83]
	ds_read_b128 v[128:131], v231 offset:28672
	v_exp_f32_e32 v108, v108
	v_exp_f32_e32 v109, v109
	v_exp_f32_e32 v110, v110
	v_exp_f32_e32 v111, v111
	v_exp_f32_e32 v112, v112
	v_exp_f32_e32 v113, v113
	v_exp_f32_e32 v114, v114
	v_exp_f32_e32 v115, v115
	s_waitcnt lgkmcnt(3)
	v_mfma_f32_32x32x16_bf16 v[68:83], v[116:119], v[164:167], v[68:83]
	v_add_f32_e32 v237, v100, v101
	v_add_f32_e32 v251, v102, v103
	v_add_f32_e32 v237, v237, v104
	v_add_f32_e32 v251, v251, v105
	v_add_f32_e32 v237, v237, v106
	v_add_f32_e32 v251, v251, v107
	v_add_f32_e32 v237, v237, v108
	v_add_f32_e32 v251, v251, v109
	s_waitcnt lgkmcnt(2)
	v_mfma_f32_32x32x16_bf16 v[68:83], v[120:123], v[172:175], v[68:83]
	v_add_f32_e32 v237, v237, v110
	v_add_f32_e32 v251, v251, v111
	v_add_f32_e32 v237, v237, v112
	v_add_f32_e32 v251, v251, v113
	v_add_f32_e32 v237, v237, v114
	v_add_f32_e32 v251, v251, v115
	v_add_f32_e32 v237, v237, v251
	v_cvt_pk_bf16_f32 v238, v100, v101
	s_waitcnt lgkmcnt(1)
	v_mfma_f32_32x32x16_bf16 v[68:83], v[124:127], v[168:171], v[68:83]
	v_cvt_pk_bf16_f32 v239, v102, v103
	v_cvt_pk_bf16_f32 v240, v104, v105
	v_cvt_pk_bf16_f32 v241, v106, v107
	v_cvt_pk_bf16_f32 v242, v108, v109
	v_cvt_pk_bf16_f32 v243, v110, v111
	v_cvt_pk_bf16_f32 v244, v112, v113
	v_cvt_pk_bf16_f32 v245, v114, v115
	s_nop 1
	s_waitcnt lgkmcnt(0)
	v_mfma_f32_32x32x16_bf16 v[68:83], v[128:131], v[176:179], v[68:83]
	v_permlane32_swap_b32_e32 v238, v240
	v_permlane32_swap_b32_e32 v239, v241
	v_permlane32_swap_b32_e32 v242, v244
	v_permlane32_swap_b32_e32 v243, v245
	ds_read_b64_tr_b16 v[116:117], v191 offset:16384
	ds_read_b64_tr_b16 v[118:119], v191 offset:18432
	ds_read_b64_tr_b16 v[120:121], v191 offset:20480
	ds_read_b64_tr_b16 v[122:123], v191 offset:22528
	ds_read_b64_tr_b16 v[124:125], v191 offset:24576
	ds_read_b64_tr_b16 v[126:127], v191 offset:26624
	ds_read_b64_tr_b16 v[128:129], v191 offset:28672
	ds_read_b64_tr_b16 v[130:131], v191 offset:30720
	s_setprio 0
	s_nop 3
	v_sub_f32_e32 v100, v68, v222
	v_sub_f32_e32 v101, v69, v222
	v_sub_f32_e32 v102, v70, v222
	v_sub_f32_e32 v103, v71, v222
	v_sub_f32_e32 v104, v72, v222
	v_sub_f32_e32 v105, v73, v222
	v_sub_f32_e32 v106, v74, v222
	v_sub_f32_e32 v107, v75, v222
	v_sub_f32_e32 v108, v76, v222
	v_sub_f32_e32 v109, v77, v222
	v_sub_f32_e32 v110, v78, v222
	v_sub_f32_e32 v111, v79, v222
	v_sub_f32_e32 v112, v80, v222
	v_sub_f32_e32 v113, v81, v222
	v_sub_f32_e32 v114, v82, v222
	v_sub_f32_e32 v115, v83, v222
	v_exp_f32_e32 v100, v100
	v_exp_f32_e32 v101, v101
	v_exp_f32_e32 v102, v102
	v_exp_f32_e32 v103, v103
	v_exp_f32_e32 v104, v104
	v_exp_f32_e32 v105, v105
	v_exp_f32_e32 v106, v106
	v_exp_f32_e32 v107, v107
	v_exp_f32_e32 v108, v108
	v_exp_f32_e32 v109, v109
	v_exp_f32_e32 v110, v110
	v_exp_f32_e32 v111, v111
	v_exp_f32_e32 v112, v112
	v_exp_f32_e32 v113, v113
	v_exp_f32_e32 v114, v114
	v_exp_f32_e32 v115, v115
	v_add_f32_e32 v250, v100, v101
	v_add_f32_e32 v251, v102, v103
	v_add_f32_e32 v250, v250, v104
	v_add_f32_e32 v251, v251, v105
	v_add_f32_e32 v250, v250, v106
	v_add_f32_e32 v251, v251, v107
	v_add_f32_e32 v250, v250, v108
	v_add_f32_e32 v251, v251, v109
	v_add_f32_e32 v250, v250, v110
	v_add_f32_e32 v251, v251, v111
	v_add_f32_e32 v250, v250, v112
	v_add_f32_e32 v251, v251, v113
	v_add_f32_e32 v250, v250, v114
	v_add_f32_e32 v251, v251, v115
	v_add_f32_e32 v250, v250, v251
	v_cvt_pk_bf16_f32 v100, v100, v101
	v_cvt_pk_bf16_f32 v101, v102, v103
	v_cvt_pk_bf16_f32 v102, v104, v105
	v_cvt_pk_bf16_f32 v103, v106, v107
	v_cvt_pk_bf16_f32 v104, v108, v109
	v_cvt_pk_bf16_f32 v105, v110, v111
	v_cvt_pk_bf16_f32 v106, v112, v113
	v_cvt_pk_bf16_f32 v107, v114, v115
	s_nop 1
	v_permlane32_swap_b32_e32 v100, v102
	v_permlane32_swap_b32_e32 v101, v103
	v_permlane32_swap_b32_e32 v104, v106
	v_permlane32_swap_b32_e32 v105, v107

.LBB0_1452:
	s_cmp_le_i32 s18, s40
	s_cbranch_scc0 .Lorig_a1b0
	s_cmp_eq_u32 s71, 0
	s_cbranch_scc1 .Lorig_a1b0
	s_setprio 3
	ds_read_b128 v[140:143], v176
	ds_read_b128 v[144:147], v176 offset:32
	ds_read_b128 v[148:151], v176 offset:64
	ds_read_b128 v[152:155], v176 offset:96
	ds_read_b128 v[208:211], v172 offset:32768
	ds_read_b128 v[212:215], v206 offset:32768
	ds_read_b128 v[216:219], v207 offset:32768
	ds_read_b128 v[220:223], v237 offset:32768
	ds_read_b128 v[224:227], v244 offset:32768
	ds_read_b128 v[228:231], v245 offset:32768
	ds_read_b128 v[232:235], v246 offset:32768
	ds_read_b128 v[238:241], v247 offset:32768
	ds_read_b128 v[156:159], v176 offset:128
	ds_read_b128 v[160:163], v176 offset:160
	ds_read_b128 v[164:167], v176 offset:192
	ds_read_b128 v[168:171], v176 offset:224
	s_waitcnt lgkmcnt(11)
	v_mfma_f32_32x32x16_bf16 v[84:99], v[208:211], v[100:103], v[140:155]
	ds_read_b128 v[208:211], v172 offset:40960
	s_waitcnt lgkmcnt(11)
	v_mfma_f32_32x32x16_bf16 v[84:99], v[212:215], v[104:107], v[84:99]
	ds_read_b128 v[212:215], v206 offset:40960
	s_waitcnt lgkmcnt(11)
	v_mfma_f32_32x32x16_bf16 v[84:99], v[216:219], v[108:111], v[84:99]
	ds_read_b128 v[216:219], v207 offset:40960
	s_waitcnt lgkmcnt(11)
	v_mfma_f32_32x32x16_bf16 v[84:99], v[220:223], v[112:115], v[84:99]
	ds_read_b128 v[220:223], v237 offset:40960
	s_waitcnt lgkmcnt(11)
	v_mfma_f32_32x32x16_bf16 v[84:99], v[224:227], v[116:119], v[84:99]
	ds_read_b128 v[224:227], v244 offset:40960
	s_waitcnt lgkmcnt(11)
	v_mfma_f32_32x32x16_bf16 v[84:99], v[228:231], v[120:123], v[84:99]
	ds_read_b128 v[228:231], v245 offset:40960
	s_waitcnt lgkmcnt(11)
	v_mfma_f32_32x32x16_bf16 v[84:99], v[232:235], v[124:127], v[84:99]
	ds_read_b128 v[232:235], v246 offset:40960
	s_waitcnt lgkmcnt(11)
	v_mfma_f32_32x32x16_bf16 v[84:99], v[238:241], v[128:131], v[84:99]
	ds_read_b128 v[238:241], v247 offset:40960
	v_cmp_eq_f32_e32 vcc, 0, v193
	s_cmp_eq_u64 vcc, exec
	s_cbranch_scc0 .Lsub_a1b0
	s_waitcnt lgkmcnt(7)
	v_mfma_f32_32x32x16_bf16 v[68:83], v[208:211], v[100:103], v[156:171]
	s_waitcnt lgkmcnt(6)
	v_mfma_f32_32x32x16_bf16 v[68:83], v[212:215], v[104:107], v[68:83]
	s_waitcnt lgkmcnt(5)
	v_mfma_f32_32x32x16_bf16 v[68:83], v[216:219], v[108:111], v[68:83]
	s_waitcnt lgkmcnt(4)
	v_mfma_f32_32x32x16_bf16 v[68:83], v[220:223], v[112:115], v[68:83]
	s_waitcnt lgkmcnt(3)
	v_mfma_f32_32x32x16_bf16 v[68:83], v[224:227], v[116:119], v[68:83]
	v_exp_f32_e32 v140, v84
	v_exp_f32_e32 v141, v85
	v_exp_f32_e32 v142, v86
	v_exp_f32_e32 v143, v87
	v_exp_f32_e32 v144, v88
	v_exp_f32_e32 v145, v89
	v_exp_f32_e32 v146, v90
	v_exp_f32_e32 v147, v91
	v_exp_f32_e32 v148, v92
	v_exp_f32_e32 v149, v93
	v_exp_f32_e32 v150, v94
	s_waitcnt lgkmcnt(2)
	v_mfma_f32_32x32x16_bf16 v[68:83], v[228:231], v[120:123], v[68:83]
	v_exp_f32_e32 v151, v95
	v_exp_f32_e32 v152, v96
	v_exp_f32_e32 v153, v97
	v_exp_f32_e32 v154, v98
	v_exp_f32_e32 v155, v99
	v_add_f32_e32 v248, v140, v141
	v_add_f32_e32 v250, v142, v143
	v_add_f32_e32 v248, v248, v144
	v_add_f32_e32 v250, v250, v145
	v_add_f32_e32 v248, v248, v146
	v_add_f32_e32 v250, v250, v147
	s_waitcnt lgkmcnt(1)
	v_mfma_f32_32x32x16_bf16 v[68:83], v[232:235], v[124:127], v[68:83]
	v_add_f32_e32 v248, v248, v148
	v_add_f32_e32 v250, v250, v149
	v_add_f32_e32 v248, v248, v150
	v_add_f32_e32 v250, v250, v151
	v_add_f32_e32 v248, v248, v152
	v_add_f32_e32 v250, v250, v153
	v_add_f32_e32 v248, v248, v154
	v_add_f32_e32 v250, v250, v155
	v_add_f32_e32 v248, v248, v250
	v_cvt_pk_bf16_f32 v140, v140, v141
	v_cvt_pk_bf16_f32 v141, v142, v143
	s_waitcnt lgkmcnt(0)
	v_mfma_f32_32x32x16_bf16 v[68:83], v[238:241], v[128:131], v[68:83]
	v_cvt_pk_bf16_f32 v142, v144, v145
	v_cvt_pk_bf16_f32 v143, v146, v147
	v_cvt_pk_bf16_f32 v144, v148, v149
	v_cvt_pk_bf16_f32 v145, v150, v151
	v_cvt_pk_bf16_f32 v146, v152, v153
	v_cvt_pk_bf16_f32 v147, v154, v155
	s_nop 1
	v_permlane32_swap_b32_e32 v140, v142
	v_permlane32_swap_b32_e32 v141, v143
	v_permlane32_swap_b32_e32 v144, v146
	v_permlane32_swap_b32_e32 v145, v147
	ds_read_b64_tr_b16 v[208:209], v174 offset:0
	ds_read_b64_tr_b16 v[210:211], v174 offset:2048
	ds_read_b64_tr_b16 v[212:213], v174 offset:4096
	ds_read_b64_tr_b16 v[214:215], v174 offset:6144
	ds_read_b64_tr_b16 v[216:217], v174 offset:8192
	ds_read_b64_tr_b16 v[218:219], v174 offset:10240
	ds_read_b64_tr_b16 v[220:221], v174 offset:12288
	ds_read_b64_tr_b16 v[222:223], v174 offset:14336
	s_setprio 0
	s_nop 3
	v_exp_f32_e32 v156, v68
	v_exp_f32_e32 v157, v69
	v_exp_f32_e32 v158, v70
	v_exp_f32_e32 v159, v71
	v_exp_f32_e32 v160, v72
	v_exp_f32_e32 v161, v73
	v_exp_f32_e32 v162, v74
	v_exp_f32_e32 v163, v75
	v_exp_f32_e32 v164, v76
	v_exp_f32_e32 v165, v77
	v_exp_f32_e32 v166, v78
	v_exp_f32_e32 v167, v79
	v_exp_f32_e32 v168, v80
	v_exp_f32_e32 v169, v81
	v_exp_f32_e32 v170, v82
	v_exp_f32_e32 v171, v83
	v_add_f32_e32 v249, v156, v157
	v_add_f32_e32 v250, v158, v159
	v_add_f32_e32 v249, v249, v160
	v_add_f32_e32 v250, v250, v161
	v_add_f32_e32 v249, v249, v162
	v_add_f32_e32 v250, v250, v163
	v_add_f32_e32 v249, v249, v164
	v_add_f32_e32 v250, v250, v165
	v_add_f32_e32 v249, v249, v166
	v_add_f32_e32 v250, v250, v167
	v_add_f32_e32 v249, v249, v168
	v_add_f32_e32 v250, v250, v169
	v_add_f32_e32 v249, v249, v170
	v_add_f32_e32 v250, v250, v171
	v_add_f32_e32 v249, v249, v250
	v_cvt_pk_bf16_f32 v156, v156, v157
	v_cvt_pk_bf16_f32 v157, v158, v159
	v_cvt_pk_bf16_f32 v158, v160, v161
	v_cvt_pk_bf16_f32 v159, v162, v163
	v_cvt_pk_bf16_f32 v160, v164, v165
	v_cvt_pk_bf16_f32 v161, v166, v167
	v_cvt_pk_bf16_f32 v162, v168, v169
	v_cvt_pk_bf16_f32 v163, v170, v171
	s_nop 1
	v_permlane32_swap_b32_e32 v156, v158
	v_permlane32_swap_b32_e32 v157, v159
	v_permlane32_swap_b32_e32 v160, v162
	v_permlane32_swap_b32_e32 v161, v163
	s_branch .Lsum_a1b0
.Lsub_a1b0:
	s_waitcnt lgkmcnt(7)
	v_mfma_f32_32x32x16_bf16 v[68:83], v[208:211], v[100:103], v[156:171]
	s_waitcnt lgkmcnt(6)
	v_mfma_f32_32x32x16_bf16 v[68:83], v[212:215], v[104:107], v[68:83]
	s_waitcnt lgkmcnt(5)
	v_mfma_f32_32x32x16_bf16 v[68:83], v[216:219], v[108:111], v[68:83]
	s_waitcnt lgkmcnt(4)
	v_mfma_f32_32x32x16_bf16 v[68:83], v[220:223], v[112:115], v[68:83]
	s_waitcnt lgkmcnt(3)
	v_mfma_f32_32x32x16_bf16 v[68:83], v[224:227], v[116:119], v[68:83]
	v_sub_f32_e32 v140, v84, v193
	v_sub_f32_e32 v141, v85, v193
	v_sub_f32_e32 v142, v86, v193
	v_sub_f32_e32 v143, v87, v193
	v_sub_f32_e32 v144, v88, v193
	v_sub_f32_e32 v145, v89, v193
	v_sub_f32_e32 v146, v90, v193
	v_sub_f32_e32 v147, v91, v193
	v_sub_f32_e32 v148, v92, v193
	v_sub_f32_e32 v149, v93, v193
	v_sub_f32_e32 v150, v94, v193
	v_sub_f32_e32 v151, v95, v193
	v_sub_f32_e32 v152, v96, v193
	v_sub_f32_e32 v153, v97, v193
	v_sub_f32_e32 v154, v98, v193
	s_waitcnt lgkmcnt(2)
	v_mfma_f32_32x32x16_bf16 v[68:83], v[228:231], v[120:123], v[68:83]
	v_sub_f32_e32 v155, v99, v193
	v_exp_f32_e32 v140, v140
	v_exp_f32_e32 v141, v141
	v_exp_f32_e32 v142, v142
	v_exp_f32_e32 v143, v143
	v_exp_f32_e32 v144, v144
	v_exp_f32_e32 v145, v145
	v_exp_f32_e32 v146, v146
	v_exp_f32_e32 v147, v147
	v_exp_f32_e32 v148, v148
	v_exp_f32_e32 v149, v149
	v_exp_f32_e32 v150, v150
	v_exp_f32_e32 v151, v151
	v_exp_f32_e32 v152, v152
	v_exp_f32_e32 v153, v153
	s_waitcnt lgkmcnt(1)
	v_mfma_f32_32x32x16_bf16 v[68:83], v[232:235], v[124:127], v[68:83]
	v_exp_f32_e32 v154, v154
	v_exp_f32_e32 v155, v155
	v_add_f32_e32 v248, v140, v141
	v_add_f32_e32 v250, v142, v143
	v_add_f32_e32 v248, v248, v144
	v_add_f32_e32 v250, v250, v145
	v_add_f32_e32 v248, v248, v146
	v_add_f32_e32 v250, v250, v147
	v_add_f32_e32 v248, v248, v148
	v_add_f32_e32 v250, v250, v149
	v_add_f32_e32 v248, v248, v150
	v_add_f32_e32 v250, v250, v151
	v_add_f32_e32 v248, v248, v152
	v_add_f32_e32 v250, v250, v153
	v_add_f32_e32 v248, v248, v154
	s_waitcnt lgkmcnt(0)
	v_mfma_f32_32x32x16_bf16 v[68:83], v[238:241], v[128:131], v[68:83]
	v_add_f32_e32 v250, v250, v155
	v_add_f32_e32 v248, v248, v250
	v_cvt_pk_bf16_f32 v140, v140, v141
	v_cvt_pk_bf16_f32 v141, v142, v143
	v_cvt_pk_bf16_f32 v142, v144, v145
	v_cvt_pk_bf16_f32 v143, v146, v147
	v_cvt_pk_bf16_f32 v144, v148, v149
	v_cvt_pk_bf16_f32 v145, v150, v151
	v_cvt_pk_bf16_f32 v146, v152, v153
	v_cvt_pk_bf16_f32 v147, v154, v155
	s_nop 1
	v_permlane32_swap_b32_e32 v140, v142
	v_permlane32_swap_b32_e32 v141, v143
	v_permlane32_swap_b32_e32 v144, v146
	v_permlane32_swap_b32_e32 v145, v147
	ds_read_b64_tr_b16 v[208:209], v174 offset:0
	ds_read_b64_tr_b16 v[210:211], v174 offset:2048
	ds_read_b64_tr_b16 v[212:213], v174 offset:4096
	ds_read_b64_tr_b16 v[214:215], v174 offset:6144
	ds_read_b64_tr_b16 v[216:217], v174 offset:8192
	ds_read_b64_tr_b16 v[218:219], v174 offset:10240
	ds_read_b64_tr_b16 v[220:221], v174 offset:12288
	ds_read_b64_tr_b16 v[222:223], v174 offset:14336
	s_setprio 0
	s_nop 3
	v_sub_f32_e32 v156, v68, v193
	v_sub_f32_e32 v157, v69, v193
	v_sub_f32_e32 v158, v70, v193
	v_sub_f32_e32 v159, v71, v193
	v_sub_f32_e32 v160, v72, v193
	v_sub_f32_e32 v161, v73, v193
	v_sub_f32_e32 v162, v74, v193
	v_sub_f32_e32 v163, v75, v193
	v_sub_f32_e32 v164, v76, v193
	v_sub_f32_e32 v165, v77, v193
	v_sub_f32_e32 v166, v78, v193
	v_sub_f32_e32 v167, v79, v193
	v_sub_f32_e32 v168, v80, v193
	v_sub_f32_e32 v169, v81, v193
	v_sub_f32_e32 v170, v82, v193
	v_sub_f32_e32 v171, v83, v193
	v_exp_f32_e32 v156, v156
	v_exp_f32_e32 v157, v157
	v_exp_f32_e32 v158, v158
	v_exp_f32_e32 v159, v159
	v_exp_f32_e32 v160, v160
	v_exp_f32_e32 v161, v161
	v_exp_f32_e32 v162, v162
	v_exp_f32_e32 v163, v163
	v_exp_f32_e32 v164, v164
	v_exp_f32_e32 v165, v165
	v_exp_f32_e32 v166, v166
	v_exp_f32_e32 v167, v167
	v_exp_f32_e32 v168, v168
	v_exp_f32_e32 v169, v169
	v_exp_f32_e32 v170, v170
	v_exp_f32_e32 v171, v171
	v_add_f32_e32 v249, v156, v157
	v_add_f32_e32 v250, v158, v159
	v_add_f32_e32 v249, v249, v160
	v_add_f32_e32 v250, v250, v161
	v_add_f32_e32 v249, v249, v162
	v_add_f32_e32 v250, v250, v163
	v_add_f32_e32 v249, v249, v164
	v_add_f32_e32 v250, v250, v165
	v_add_f32_e32 v249, v249, v166
	v_add_f32_e32 v250, v250, v167
	v_add_f32_e32 v249, v249, v168
	v_add_f32_e32 v250, v250, v169
	v_add_f32_e32 v249, v249, v170
	v_add_f32_e32 v250, v250, v171
	v_add_f32_e32 v249, v249, v250
	v_cvt_pk_bf16_f32 v156, v156, v157
	v_cvt_pk_bf16_f32 v157, v158, v159
	v_cvt_pk_bf16_f32 v158, v160, v161
	v_cvt_pk_bf16_f32 v159, v162, v163
	v_cvt_pk_bf16_f32 v160, v164, v165
	v_cvt_pk_bf16_f32 v161, v166, v167
	v_cvt_pk_bf16_f32 v162, v168, v169
	v_cvt_pk_bf16_f32 v163, v170, v171
	s_nop 1
	v_permlane32_swap_b32_e32 v156, v158
	v_permlane32_swap_b32_e32 v157, v159
	v_permlane32_swap_b32_e32 v160, v162
	v_permlane32_swap_b32_e32 v161, v163

.LBB0_1467:
	s_add_i32 s98, s18, 64
	s_cmp_le_i32 s98, s40
	s_cbranch_scc0 .Lorig_a1b1
	s_setprio 3
	ds_read_b128 v[140:143], v177
	ds_read_b128 v[144:147], v177 offset:32
	ds_read_b128 v[148:151], v177 offset:64
	ds_read_b128 v[152:155], v177 offset:96
	ds_read_b128 v[208:211], v172 offset:49152
	ds_read_b128 v[212:215], v206 offset:49152
	ds_read_b128 v[216:219], v207 offset:49152
	ds_read_b128 v[220:223], v237 offset:49152
	ds_read_b128 v[224:227], v244 offset:49152
	ds_read_b128 v[228:231], v245 offset:49152
	ds_read_b128 v[232:235], v246 offset:49152
	ds_read_b128 v[238:241], v247 offset:49152
	ds_read_b128 v[156:159], v177 offset:128
	ds_read_b128 v[160:163], v177 offset:160
	ds_read_b128 v[164:167], v177 offset:192
	ds_read_b128 v[168:171], v177 offset:224
	s_waitcnt lgkmcnt(11)
	v_mfma_f32_32x32x16_bf16 v[84:99], v[208:211], v[100:103], v[140:155]
	ds_read_b128 v[208:211], v172 offset:57344
	s_waitcnt lgkmcnt(11)
	v_mfma_f32_32x32x16_bf16 v[84:99], v[212:215], v[104:107], v[84:99]
	ds_read_b128 v[212:215], v206 offset:57344
	s_waitcnt lgkmcnt(11)
	v_mfma_f32_32x32x16_bf16 v[84:99], v[216:219], v[108:111], v[84:99]
	ds_read_b128 v[216:219], v207 offset:57344
	s_waitcnt lgkmcnt(11)
	v_mfma_f32_32x32x16_bf16 v[84:99], v[220:223], v[112:115], v[84:99]
	ds_read_b128 v[220:223], v237 offset:57344
	s_waitcnt lgkmcnt(11)
	v_mfma_f32_32x32x16_bf16 v[84:99], v[224:227], v[116:119], v[84:99]
	ds_read_b128 v[224:227], v244 offset:57344
	s_waitcnt lgkmcnt(11)
	v_mfma_f32_32x32x16_bf16 v[84:99], v[228:231], v[120:123], v[84:99]
	ds_read_b128 v[228:231], v245 offset:57344
	s_waitcnt lgkmcnt(11)
	v_mfma_f32_32x32x16_bf16 v[84:99], v[232:235], v[124:127], v[84:99]
	ds_read_b128 v[232:235], v246 offset:57344
	s_waitcnt lgkmcnt(11)
	v_mfma_f32_32x32x16_bf16 v[84:99], v[238:241], v[128:131], v[84:99]
	ds_read_b128 v[238:241], v247 offset:57344
	v_cmp_eq_f32_e32 vcc, 0, v192
	s_cmp_eq_u64 vcc, exec
	s_cbranch_scc0 .Lsub_a1b1
	s_waitcnt lgkmcnt(7)
	v_mfma_f32_32x32x16_bf16 v[68:83], v[208:211], v[100:103], v[156:171]
	s_waitcnt lgkmcnt(6)
	v_mfma_f32_32x32x16_bf16 v[68:83], v[212:215], v[104:107], v[68:83]
	s_waitcnt lgkmcnt(5)
	v_mfma_f32_32x32x16_bf16 v[68:83], v[216:219], v[108:111], v[68:83]
	s_waitcnt lgkmcnt(4)
	v_mfma_f32_32x32x16_bf16 v[68:83], v[220:223], v[112:115], v[68:83]
	s_waitcnt lgkmcnt(3)
	v_mfma_f32_32x32x16_bf16 v[68:83], v[224:227], v[116:119], v[68:83]
	v_exp_f32_e32 v140, v84
	v_exp_f32_e32 v141, v85
	v_exp_f32_e32 v142, v86
	v_exp_f32_e32 v143, v87
	v_exp_f32_e32 v144, v88
	v_exp_f32_e32 v145, v89
	v_exp_f32_e32 v146, v90
	v_exp_f32_e32 v147, v91
	v_exp_f32_e32 v148, v92
	v_exp_f32_e32 v149, v93
	v_exp_f32_e32 v150, v94
	s_waitcnt lgkmcnt(2)
	v_mfma_f32_32x32x16_bf16 v[68:83], v[228:231], v[120:123], v[68:83]
	v_exp_f32_e32 v151, v95
	v_exp_f32_e32 v152, v96
	v_exp_f32_e32 v153, v97
	v_exp_f32_e32 v154, v98
	v_exp_f32_e32 v155, v99
	v_add_f32_e32 v248, v140, v141
	v_add_f32_e32 v250, v142, v143
	v_add_f32_e32 v248, v248, v144
	v_add_f32_e32 v250, v250, v145
	v_add_f32_e32 v248, v248, v146
	v_add_f32_e32 v250, v250, v147
	s_waitcnt lgkmcnt(1)
	v_mfma_f32_32x32x16_bf16 v[68:83], v[232:235], v[124:127], v[68:83]
	v_add_f32_e32 v248, v248, v148
	v_add_f32_e32 v250, v250, v149
	v_add_f32_e32 v248, v248, v150
	v_add_f32_e32 v250, v250, v151
	v_add_f32_e32 v248, v248, v152
	v_add_f32_e32 v250, v250, v153
	v_add_f32_e32 v248, v248, v154
	v_add_f32_e32 v250, v250, v155
	v_add_f32_e32 v248, v248, v250
	v_cvt_pk_bf16_f32 v140, v140, v141
	v_cvt_pk_bf16_f32 v141, v142, v143
	s_waitcnt lgkmcnt(0)
	v_mfma_f32_32x32x16_bf16 v[68:83], v[238:241], v[128:131], v[68:83]
	v_cvt_pk_bf16_f32 v142, v144, v145
	v_cvt_pk_bf16_f32 v143, v146, v147
	v_cvt_pk_bf16_f32 v144, v148, v149
	v_cvt_pk_bf16_f32 v145, v150, v151
	v_cvt_pk_bf16_f32 v146, v152, v153
	v_cvt_pk_bf16_f32 v147, v154, v155
	s_nop 1
	v_permlane32_swap_b32_e32 v140, v142
	v_permlane32_swap_b32_e32 v141, v143
	v_permlane32_swap_b32_e32 v144, v146
	v_permlane32_swap_b32_e32 v145, v147
	ds_read_b64_tr_b16 v[208:209], v174 offset:16384
	ds_read_b64_tr_b16 v[210:211], v174 offset:18432
	ds_read_b64_tr_b16 v[212:213], v174 offset:20480
	ds_read_b64_tr_b16 v[214:215], v174 offset:22528
	ds_read_b64_tr_b16 v[216:217], v174 offset:24576
	ds_read_b64_tr_b16 v[218:219], v174 offset:26624
	ds_read_b64_tr_b16 v[220:221], v174 offset:28672
	ds_read_b64_tr_b16 v[222:223], v174 offset:30720
	s_setprio 0
	s_nop 3
	v_exp_f32_e32 v156, v68
	v_exp_f32_e32 v157, v69
	v_exp_f32_e32 v158, v70
	v_exp_f32_e32 v159, v71
	v_exp_f32_e32 v160, v72
	v_exp_f32_e32 v161, v73
	v_exp_f32_e32 v162, v74
	v_exp_f32_e32 v163, v75
	v_exp_f32_e32 v164, v76
	v_exp_f32_e32 v165, v77
	v_exp_f32_e32 v166, v78
	v_exp_f32_e32 v167, v79
	v_exp_f32_e32 v168, v80
	v_exp_f32_e32 v169, v81
	v_exp_f32_e32 v170, v82
	v_exp_f32_e32 v171, v83
	v_add_f32_e32 v249, v156, v157
	v_add_f32_e32 v250, v158, v159
	v_add_f32_e32 v249, v249, v160
	v_add_f32_e32 v250, v250, v161
	v_add_f32_e32 v249, v249, v162
	v_add_f32_e32 v250, v250, v163
	v_add_f32_e32 v249, v249, v164
	v_add_f32_e32 v250, v250, v165
	v_add_f32_e32 v249, v249, v166
	v_add_f32_e32 v250, v250, v167
	v_add_f32_e32 v249, v249, v168
	v_add_f32_e32 v250, v250, v169
	v_add_f32_e32 v249, v249, v170
	v_add_f32_e32 v250, v250, v171
	v_add_f32_e32 v249, v249, v250
	v_cvt_pk_bf16_f32 v156, v156, v157
	v_cvt_pk_bf16_f32 v157, v158, v159
	v_cvt_pk_bf16_f32 v158, v160, v161
	v_cvt_pk_bf16_f32 v159, v162, v163
	v_cvt_pk_bf16_f32 v160, v164, v165
	v_cvt_pk_bf16_f32 v161, v166, v167
	v_cvt_pk_bf16_f32 v162, v168, v169
	v_cvt_pk_bf16_f32 v163, v170, v171
	s_nop 1
	v_permlane32_swap_b32_e32 v156, v158
	v_permlane32_swap_b32_e32 v157, v159
	v_permlane32_swap_b32_e32 v160, v162
	v_permlane32_swap_b32_e32 v161, v163
	s_branch .Lsum_a1b1
.Lsub_a1b1:
	s_waitcnt lgkmcnt(7)
	v_mfma_f32_32x32x16_bf16 v[68:83], v[208:211], v[100:103], v[156:171]
	s_waitcnt lgkmcnt(6)
	v_mfma_f32_32x32x16_bf16 v[68:83], v[212:215], v[104:107], v[68:83]
	s_waitcnt lgkmcnt(5)
	v_mfma_f32_32x32x16_bf16 v[68:83], v[216:219], v[108:111], v[68:83]
	s_waitcnt lgkmcnt(4)
	v_mfma_f32_32x32x16_bf16 v[68:83], v[220:223], v[112:115], v[68:83]
	s_waitcnt lgkmcnt(3)
	v_mfma_f32_32x32x16_bf16 v[68:83], v[224:227], v[116:119], v[68:83]
	v_sub_f32_e32 v140, v84, v192
	v_sub_f32_e32 v141, v85, v192
	v_sub_f32_e32 v142, v86, v192
	v_sub_f32_e32 v143, v87, v192
	v_sub_f32_e32 v144, v88, v192
	v_sub_f32_e32 v145, v89, v192
	v_sub_f32_e32 v146, v90, v192
	v_sub_f32_e32 v147, v91, v192
	v_sub_f32_e32 v148, v92, v192
	v_sub_f32_e32 v149, v93, v192
	v_sub_f32_e32 v150, v94, v192
	v_sub_f32_e32 v151, v95, v192
	v_sub_f32_e32 v152, v96, v192
	v_sub_f32_e32 v153, v97, v192
	v_sub_f32_e32 v154, v98, v192
	s_waitcnt lgkmcnt(2)
	v_mfma_f32_32x32x16_bf16 v[68:83], v[228:231], v[120:123], v[68:83]
	v_sub_f32_e32 v155, v99, v192
	v_exp_f32_e32 v140, v140
	v_exp_f32_e32 v141, v141
	v_exp_f32_e32 v142, v142
	v_exp_f32_e32 v143, v143
	v_exp_f32_e32 v144, v144
	v_exp_f32_e32 v145, v145
	v_exp_f32_e32 v146, v146
	v_exp_f32_e32 v147, v147
	v_exp_f32_e32 v148, v148
	v_exp_f32_e32 v149, v149
	v_exp_f32_e32 v150, v150
	v_exp_f32_e32 v151, v151
	v_exp_f32_e32 v152, v152
	v_exp_f32_e32 v153, v153
	s_waitcnt lgkmcnt(1)
	v_mfma_f32_32x32x16_bf16 v[68:83], v[232:235], v[124:127], v[68:83]
	v_exp_f32_e32 v154, v154
	v_exp_f32_e32 v155, v155
	v_add_f32_e32 v248, v140, v141
	v_add_f32_e32 v250, v142, v143
	v_add_f32_e32 v248, v248, v144
	v_add_f32_e32 v250, v250, v145
	v_add_f32_e32 v248, v248, v146
	v_add_f32_e32 v250, v250, v147
	v_add_f32_e32 v248, v248, v148
	v_add_f32_e32 v250, v250, v149
	v_add_f32_e32 v248, v248, v150
	v_add_f32_e32 v250, v250, v151
	v_add_f32_e32 v248, v248, v152
	v_add_f32_e32 v250, v250, v153
	v_add_f32_e32 v248, v248, v154
	s_waitcnt lgkmcnt(0)
	v_mfma_f32_32x32x16_bf16 v[68:83], v[238:241], v[128:131], v[68:83]
	v_add_f32_e32 v250, v250, v155
	v_add_f32_e32 v248, v248, v250
	v_cvt_pk_bf16_f32 v140, v140, v141
	v_cvt_pk_bf16_f32 v141, v142, v143
	v_cvt_pk_bf16_f32 v142, v144, v145
	v_cvt_pk_bf16_f32 v143, v146, v147
	v_cvt_pk_bf16_f32 v144, v148, v149
	v_cvt_pk_bf16_f32 v145, v150, v151
	v_cvt_pk_bf16_f32 v146, v152, v153
	v_cvt_pk_bf16_f32 v147, v154, v155
	s_nop 1
	v_permlane32_swap_b32_e32 v140, v142
	v_permlane32_swap_b32_e32 v141, v143
	v_permlane32_swap_b32_e32 v144, v146
	v_permlane32_swap_b32_e32 v145, v147
	ds_read_b64_tr_b16 v[208:209], v174 offset:16384
	ds_read_b64_tr_b16 v[210:211], v174 offset:18432
	ds_read_b64_tr_b16 v[212:213], v174 offset:20480
	ds_read_b64_tr_b16 v[214:215], v174 offset:22528
	ds_read_b64_tr_b16 v[216:217], v174 offset:24576
	ds_read_b64_tr_b16 v[218:219], v174 offset:26624
	ds_read_b64_tr_b16 v[220:221], v174 offset:28672
	ds_read_b64_tr_b16 v[222:223], v174 offset:30720
	s_setprio 0
	s_nop 3
	v_sub_f32_e32 v156, v68, v192
	v_sub_f32_e32 v157, v69, v192
	v_sub_f32_e32 v158, v70, v192
	v_sub_f32_e32 v159, v71, v192
	v_sub_f32_e32 v160, v72, v192
	v_sub_f32_e32 v161, v73, v192
	v_sub_f32_e32 v162, v74, v192
	v_sub_f32_e32 v163, v75, v192
	v_sub_f32_e32 v164, v76, v192
	v_sub_f32_e32 v165, v77, v192
	v_sub_f32_e32 v166, v78, v192
	v_sub_f32_e32 v167, v79, v192
	v_sub_f32_e32 v168, v80, v192
	v_sub_f32_e32 v169, v81, v192
	v_sub_f32_e32 v170, v82, v192
	v_sub_f32_e32 v171, v83, v192
	v_exp_f32_e32 v156, v156
	v_exp_f32_e32 v157, v157
	v_exp_f32_e32 v158, v158
	v_exp_f32_e32 v159, v159
	v_exp_f32_e32 v160, v160
	v_exp_f32_e32 v161, v161
	v_exp_f32_e32 v162, v162
	v_exp_f32_e32 v163, v163
	v_exp_f32_e32 v164, v164
	v_exp_f32_e32 v165, v165
	v_exp_f32_e32 v166, v166
	v_exp_f32_e32 v167, v167
	v_exp_f32_e32 v168, v168
	v_exp_f32_e32 v169, v169
	v_exp_f32_e32 v170, v170
	v_exp_f32_e32 v171, v171
	v_add_f32_e32 v249, v156, v157
	v_add_f32_e32 v250, v158, v159
	v_add_f32_e32 v249, v249, v160
	v_add_f32_e32 v250, v250, v161
	v_add_f32_e32 v249, v249, v162
	v_add_f32_e32 v250, v250, v163
	v_add_f32_e32 v249, v249, v164
	v_add_f32_e32 v250, v250, v165
	v_add_f32_e32 v249, v249, v166
	v_add_f32_e32 v250, v250, v167
	v_add_f32_e32 v249, v249, v168
	v_add_f32_e32 v250, v250, v169
	v_add_f32_e32 v249, v249, v170
	v_add_f32_e32 v250, v250, v171
	v_add_f32_e32 v249, v249, v250
	v_cvt_pk_bf16_f32 v156, v156, v157
	v_cvt_pk_bf16_f32 v157, v158, v159
	v_cvt_pk_bf16_f32 v158, v160, v161
	v_cvt_pk_bf16_f32 v159, v162, v163
	v_cvt_pk_bf16_f32 v160, v164, v165
	v_cvt_pk_bf16_f32 v161, v166, v167
	v_cvt_pk_bf16_f32 v162, v168, v169
	v_cvt_pk_bf16_f32 v163, v170, v171
	s_nop 1
	v_permlane32_swap_b32_e32 v156, v158
	v_permlane32_swap_b32_e32 v157, v159
	v_permlane32_swap_b32_e32 v160, v162
	v_permlane32_swap_b32_e32 v161, v163
